# speedup vs baseline: 1.0150x; 1.0150x over previous
.LBB1_14:
	v_add_u32_e32 v118, s4, v224
	ds_read_b128 v[66:69], v118
	ds_read_b128 v[98:101], v218 offset:8192
	ds_read_b128 v[102:105], v118 offset:32
	ds_read_b128 v[82:85], v118 offset:384
	ds_read_b128 v[86:89], v118 offset:416
	ds_read_b128 v[90:93], v118 offset:448
	ds_read_b128 v[94:97], v118 offset:480
	s_waitcnt lgkmcnt(6)
	v_pk_add_f16 v66, v142, v66
	v_pk_add_f16 v67, v143, v67
	v_pk_add_f16 v68, v144, v68
	v_pk_add_f16 v69, v145, v69
	v_or_b32_e32 v71, 0x80008000, v68
	v_or_b32_e32 v70, 0x80008000, v69
	v_or_b32_e32 v72, 0x80008000, v67
	v_or_b32_e32 v73, 0x80008000, v66
	v_pk_fma_f16 v74, v73, s3, v221 op_sel_hi:[1,0,0]
	v_pk_fma_f16 v75, v72, s3, v221 op_sel_hi:[1,0,0]
	v_pk_fma_f16 v76, v71, s3, v221 op_sel_hi:[1,0,0]
	v_pk_fma_f16 v77, v70, s3, v221 op_sel_hi:[1,0,0]
	v_pk_fma_f16 v76, v76, v71, s20 op_sel_hi:[1,1,0]
	v_pk_fma_f16 v77, v77, v70, s20 op_sel_hi:[1,1,0]
	v_pk_fma_f16 v75, v75, v72, s20 op_sel_hi:[1,1,0]
	v_pk_fma_f16 v74, v74, v73, s20 op_sel_hi:[1,1,0]
	v_pk_fma_f16 v75, v75, v72, s21 op_sel_hi:[1,1,0]
	v_pk_fma_f16 v74, v74, v73, s21 op_sel_hi:[1,1,0]
	v_pk_fma_f16 v76, v76, v71, s21 op_sel_hi:[1,1,0]
	v_pk_fma_f16 v77, v77, v70, s21 op_sel_hi:[1,1,0]
	v_pk_max_f16 v66, v66, 0
	v_exp_f16_e32 v78, v74
	v_exp_f16_e32 v79, v75
	v_exp_f16_e32 v80, v76
	v_exp_f16_e32 v81, v77
	v_exp_f16_sdwa v78, v74 dst_sel:WORD_1 dst_unused:UNUSED_PRESERVE src0_sel:WORD_1
	v_exp_f16_sdwa v79, v75 dst_sel:WORD_1 dst_unused:UNUSED_PRESERVE src0_sel:WORD_1
	v_exp_f16_sdwa v80, v76 dst_sel:WORD_1 dst_unused:UNUSED_PRESERVE src0_sel:WORD_1
	v_exp_f16_sdwa v81, v77 dst_sel:WORD_1 dst_unused:UNUSED_PRESERVE src0_sel:WORD_1
	v_pk_max_f16 v67, v67, 0
	v_pk_max_f16 v68, v68, 0
	v_pk_max_f16 v69, v69, 0
	v_pk_fma_f16 v108, v71, v80, v68
	v_pk_fma_f16 v109, v70, v81, v69
	v_pk_fma_f16 v107, v72, v79, v67
	v_pk_fma_f16 v106, v73, v78, v66
	ds_read_b128 v[66:69], v118 offset:512
	ds_read_b128 v[70:73], v118 offset:544
	ds_read_b128 v[74:77], v118 offset:576
	ds_read_b128 v[78:81], v118 offset:608
	ds_read_b128 v[110:113], v218 offset:9216
	s_waitcnt lgkmcnt(5)
	v_mfma_f32_32x32x16_f16 v[82:97], v[150:153], v[106:109], v[82:97]
	s_waitcnt lgkmcnt(1)
	v_mfma_f32_32x32x16_f16 v[66:81], v[98:101], v[106:109], v[66:81]
	v_pk_add_f16 v98, v146, v102
	v_pk_add_f16 v99, v147, v103
	v_pk_add_f16 v100, v148, v104
	v_pk_add_f16 v101, v149, v105
	v_or_b32_e32 v103, 0x80008000, v100
	v_or_b32_e32 v102, 0x80008000, v101
	v_or_b32_e32 v104, 0x80008000, v99
	v_or_b32_e32 v105, 0x80008000, v98
	v_pk_fma_f16 v106, v105, s3, v221 op_sel_hi:[1,0,0]
	v_pk_fma_f16 v107, v104, s3, v221 op_sel_hi:[1,0,0]
	v_pk_fma_f16 v108, v103, s3, v221 op_sel_hi:[1,0,0]
	v_pk_fma_f16 v109, v102, s3, v221 op_sel_hi:[1,0,0]
	v_pk_fma_f16 v108, v108, v103, s20 op_sel_hi:[1,1,0]
	v_pk_fma_f16 v109, v109, v102, s20 op_sel_hi:[1,1,0]
	v_pk_fma_f16 v107, v107, v104, s20 op_sel_hi:[1,1,0]
	v_pk_fma_f16 v106, v106, v105, s20 op_sel_hi:[1,1,0]
	v_pk_fma_f16 v107, v107, v104, s21 op_sel_hi:[1,1,0]
	v_pk_fma_f16 v106, v106, v105, s21 op_sel_hi:[1,1,0]
	v_pk_fma_f16 v108, v108, v103, s21 op_sel_hi:[1,1,0]
	v_pk_fma_f16 v109, v109, v102, s21 op_sel_hi:[1,1,0]
	v_pk_max_f16 v98, v98, 0
	v_pk_max_f16 v99, v99, 0
	v_pk_max_f16 v100, v100, 0
	v_pk_max_f16 v101, v101, 0
	v_exp_f16_e32 v114, v106
	v_exp_f16_e32 v115, v107
	v_exp_f16_e32 v116, v108
	v_exp_f16_e32 v117, v109
	v_exp_f16_sdwa v114, v106 dst_sel:WORD_1 dst_unused:UNUSED_PRESERVE src0_sel:WORD_1
	v_exp_f16_sdwa v115, v107 dst_sel:WORD_1 dst_unused:UNUSED_PRESERVE src0_sel:WORD_1
	v_exp_f16_sdwa v116, v108 dst_sel:WORD_1 dst_unused:UNUSED_PRESERVE src0_sel:WORD_1
	v_exp_f16_sdwa v117, v109 dst_sel:WORD_1 dst_unused:UNUSED_PRESERVE src0_sel:WORD_1
	s_nop 0
	v_pk_fma_f16 v101, v102, v117, v101
	v_pk_fma_f16 v100, v103, v116, v100
	v_pk_fma_f16 v99, v104, v115, v99
	v_pk_fma_f16 v98, v105, v114, v98
	ds_read_b128 v[102:105], v118 offset:64
	ds_read_b128 v[106:109], v218 offset:2048
	v_mfma_f32_32x32x16_f16 v[82:97], v[154:157], v[98:101], v[82:97]
	v_add_u32_e32 v225, s4, v223
	ds_read_b128 v[126:129], v225
	ds_read_b128 v[130:133], v225 offset:16
	ds_read_b128 v[134:137], v225 offset:32
	ds_read_b128 v[138:141], v225 offset:48
	ds_read_b128 v[150:153], v218 offset:19456
	ds_read_b128 v[154:157], v218 offset:20480
	s_waitcnt lgkmcnt(7)
	v_pk_add_f16 v102, v158, v102
	v_pk_add_f16 v103, v159, v103
	v_pk_add_f16 v104, v160, v104
	v_pk_add_f16 v105, v161, v105
	v_mfma_f32_32x32x16_f16 v[66:81], v[110:113], v[98:101], v[66:81]
	s_setprio 0
	v_or_b32_e32 v110, 0x80008000, v105
	v_or_b32_e32 v111, 0x80008000, v104
	v_or_b32_e32 v112, 0x80008000, v103
	v_or_b32_e32 v113, 0x80008000, v102
	v_pk_fma_f16 v114, v113, s3, v221 op_sel_hi:[1,0,0]
	v_pk_fma_f16 v115, v112, s3, v221 op_sel_hi:[1,0,0]
	v_pk_fma_f16 v116, v111, s3, v221 op_sel_hi:[1,0,0]
	v_pk_fma_f16 v117, v110, s3, v221 op_sel_hi:[1,0,0]
	ds_read_b128 v[98:101], v118 offset:96
	v_pk_fma_f16 v117, v117, v110, s20 op_sel_hi:[1,1,0]
	v_pk_fma_f16 v116, v116, v111, s20 op_sel_hi:[1,1,0]
	v_pk_fma_f16 v115, v115, v112, s20 op_sel_hi:[1,1,0]
	v_pk_fma_f16 v114, v114, v113, s20 op_sel_hi:[1,1,0]
	v_pk_max_f16 v102, v102, 0
	v_pk_max_f16 v103, v103, 0
	v_pk_max_f16 v104, v104, 0
	v_pk_max_f16 v105, v105, 0
	v_pk_fma_f16 v114, v114, v113, s21 op_sel_hi:[1,1,0]
	v_pk_fma_f16 v115, v115, v112, s21 op_sel_hi:[1,1,0]
	v_pk_fma_f16 v116, v116, v111, s21 op_sel_hi:[1,1,0]
	v_pk_fma_f16 v117, v117, v110, s21 op_sel_hi:[1,1,0]
	s_nop 0
	v_exp_f16_e32 v119, v114
	v_exp_f16_e32 v120, v115
	v_exp_f16_e32 v121, v116
	v_exp_f16_e32 v122, v117
	v_exp_f16_sdwa v119, v114 dst_sel:WORD_1 dst_unused:UNUSED_PRESERVE src0_sel:WORD_1
	v_exp_f16_sdwa v120, v115 dst_sel:WORD_1 dst_unused:UNUSED_PRESERVE src0_sel:WORD_1
	v_exp_f16_sdwa v121, v116 dst_sel:WORD_1 dst_unused:UNUSED_PRESERVE src0_sel:WORD_1
	v_exp_f16_sdwa v122, v117 dst_sel:WORD_1 dst_unused:UNUSED_PRESERVE src0_sel:WORD_1
	s_nop 0
	v_pk_fma_f16 v105, v110, v122, v105
	v_pk_fma_f16 v104, v111, v121, v104
	v_pk_fma_f16 v103, v112, v120, v103
	v_pk_fma_f16 v102, v113, v119, v102
	ds_read_b128 v[110:113], v218 offset:3072
	s_waitcnt lgkmcnt(1)
	v_pk_add_f16 v98, v162, v98
	v_mfma_f32_32x32x16_f16 v[82:97], v[106:109], v[102:105], v[82:97]
	ds_read_b128 v[106:109], v218 offset:10240
	ds_read_b128 v[114:117], v218 offset:11264
	v_pk_add_f16 v99, v163, v99
	v_pk_add_f16 v100, v164, v100
	v_pk_add_f16 v101, v165, v101
	s_waitcnt lgkmcnt(1)
	v_mfma_f32_32x32x16_f16 v[66:81], v[106:109], v[102:105], v[66:81]
	v_or_b32_e32 v102, 0x80008000, v101
	v_or_b32_e32 v103, 0x80008000, v100
	v_or_b32_e32 v104, 0x80008000, v99
	v_or_b32_e32 v105, 0x80008000, v98
	v_pk_fma_f16 v106, v105, s3, v221 op_sel_hi:[1,0,0]
	v_pk_fma_f16 v107, v104, s3, v221 op_sel_hi:[1,0,0]
	v_pk_fma_f16 v108, v103, s3, v221 op_sel_hi:[1,0,0]
	v_pk_fma_f16 v109, v102, s3, v221 op_sel_hi:[1,0,0]
	v_pk_fma_f16 v108, v108, v103, s20 op_sel_hi:[1,1,0]
	v_pk_fma_f16 v109, v109, v102, s20 op_sel_hi:[1,1,0]
	v_pk_fma_f16 v107, v107, v104, s20 op_sel_hi:[1,1,0]
	v_pk_fma_f16 v106, v106, v105, s20 op_sel_hi:[1,1,0]
	v_pk_fma_f16 v107, v107, v104, s21 op_sel_hi:[1,1,0]
	v_pk_fma_f16 v106, v106, v105, s21 op_sel_hi:[1,1,0]
	v_pk_fma_f16 v108, v108, v103, s21 op_sel_hi:[1,1,0]
	v_pk_fma_f16 v109, v109, v102, s21 op_sel_hi:[1,1,0]
	v_pk_max_f16 v98, v98, 0
	v_pk_max_f16 v99, v99, 0
	v_pk_max_f16 v100, v100, 0
	v_pk_max_f16 v101, v101, 0
	v_exp_f16_e32 v119, v106
	v_exp_f16_e32 v120, v107
	v_exp_f16_e32 v121, v108
	v_exp_f16_e32 v122, v109
	v_exp_f16_sdwa v119, v106 dst_sel:WORD_1 dst_unused:UNUSED_PRESERVE src0_sel:WORD_1
	v_exp_f16_sdwa v120, v107 dst_sel:WORD_1 dst_unused:UNUSED_PRESERVE src0_sel:WORD_1
	v_exp_f16_sdwa v121, v108 dst_sel:WORD_1 dst_unused:UNUSED_PRESERVE src0_sel:WORD_1
	v_exp_f16_sdwa v122, v109 dst_sel:WORD_1 dst_unused:UNUSED_PRESERVE src0_sel:WORD_1
	s_nop 0
	v_pk_fma_f16 v101, v102, v122, v101
	v_pk_fma_f16 v100, v103, v121, v100
	v_pk_fma_f16 v99, v104, v120, v99
	v_pk_fma_f16 v98, v105, v119, v98
	ds_read_b128 v[102:105], v118 offset:128
	ds_read_b128 v[106:109], v218 offset:4096
	v_mfma_f32_32x32x16_f16 v[82:97], v[110:113], v[98:101], v[82:97]
	s_waitcnt lgkmcnt(1)
	v_pk_add_f16 v102, v166, v102
	v_pk_add_f16 v103, v167, v103
	v_pk_add_f16 v104, v168, v104
	v_pk_add_f16 v105, v169, v105
	v_or_b32_e32 v111, 0x80008000, v104
	v_mfma_f32_32x32x16_f16 v[66:81], v[114:117], v[98:101], v[66:81]
	ds_read_b128 v[226:229], v222
	ds_read_b128 v[230:233], v222 offset:1024
	ds_read_b128 v[234:237], v222 offset:2048
	ds_read_b128 v[238:241], v222 offset:3072
	v_or_b32_e32 v110, 0x80008000, v105
	v_or_b32_e32 v112, 0x80008000, v103
	v_or_b32_e32 v113, 0x80008000, v102
	v_pk_fma_f16 v114, v113, s3, v221 op_sel_hi:[1,0,0]
	v_pk_fma_f16 v115, v112, s3, v221 op_sel_hi:[1,0,0]
	v_pk_fma_f16 v116, v111, s3, v221 op_sel_hi:[1,0,0]
	v_pk_fma_f16 v117, v110, s3, v221 op_sel_hi:[1,0,0]
	ds_read_b128 v[98:101], v118 offset:160
	v_pk_fma_f16 v117, v117, v110, s20 op_sel_hi:[1,1,0]
	v_pk_fma_f16 v116, v116, v111, s20 op_sel_hi:[1,1,0]
	v_pk_fma_f16 v115, v115, v112, s20 op_sel_hi:[1,1,0]
	v_pk_fma_f16 v114, v114, v113, s20 op_sel_hi:[1,1,0]
	v_pk_max_f16 v102, v102, 0
	v_pk_max_f16 v103, v103, 0
	v_pk_max_f16 v104, v104, 0
	v_pk_max_f16 v105, v105, 0
	v_pk_fma_f16 v114, v114, v113, s21 op_sel_hi:[1,1,0]
	v_pk_fma_f16 v115, v115, v112, s21 op_sel_hi:[1,1,0]
	v_pk_fma_f16 v116, v116, v111, s21 op_sel_hi:[1,1,0]
	v_pk_fma_f16 v117, v117, v110, s21 op_sel_hi:[1,1,0]
	s_nop 0
	v_exp_f16_e32 v119, v114
	v_exp_f16_e32 v120, v115
	v_exp_f16_e32 v121, v116
	v_exp_f16_e32 v122, v117
	v_exp_f16_sdwa v119, v114 dst_sel:WORD_1 dst_unused:UNUSED_PRESERVE src0_sel:WORD_1
	v_exp_f16_sdwa v120, v115 dst_sel:WORD_1 dst_unused:UNUSED_PRESERVE src0_sel:WORD_1
	v_exp_f16_sdwa v121, v116 dst_sel:WORD_1 dst_unused:UNUSED_PRESERVE src0_sel:WORD_1
	v_exp_f16_sdwa v122, v117 dst_sel:WORD_1 dst_unused:UNUSED_PRESERVE src0_sel:WORD_1
	s_nop 0
	v_pk_fma_f16 v105, v110, v122, v105
	v_pk_fma_f16 v104, v111, v121, v104
	v_pk_fma_f16 v103, v112, v120, v103
	v_pk_fma_f16 v102, v113, v119, v102
	ds_read_b128 v[110:113], v218 offset:5120
	s_waitcnt lgkmcnt(1)
	v_pk_add_f16 v98, v170, v98
	v_mfma_f32_32x32x16_f16 v[82:97], v[106:109], v[102:105], v[82:97]
	ds_read_b128 v[106:109], v218 offset:12288
	ds_read_b128 v[114:117], v218 offset:13312
	v_pk_add_f16 v99, v171, v99
	v_pk_add_f16 v100, v172, v100
	v_pk_add_f16 v101, v173, v101
	s_waitcnt lgkmcnt(1)
	v_mfma_f32_32x32x16_f16 v[66:81], v[106:109], v[102:105], v[66:81]
	v_or_b32_e32 v102, 0x80008000, v101
	v_or_b32_e32 v103, 0x80008000, v100
	v_or_b32_e32 v104, 0x80008000, v99
	v_or_b32_e32 v105, 0x80008000, v98
	v_pk_fma_f16 v106, v105, s3, v221 op_sel_hi:[1,0,0]
	v_pk_fma_f16 v107, v104, s3, v221 op_sel_hi:[1,0,0]
	v_pk_fma_f16 v108, v103, s3, v221 op_sel_hi:[1,0,0]
	v_pk_fma_f16 v109, v102, s3, v221 op_sel_hi:[1,0,0]
	v_pk_fma_f16 v108, v108, v103, s20 op_sel_hi:[1,1,0]
	v_pk_fma_f16 v109, v109, v102, s20 op_sel_hi:[1,1,0]
	v_pk_fma_f16 v107, v107, v104, s20 op_sel_hi:[1,1,0]
	v_pk_fma_f16 v106, v106, v105, s20 op_sel_hi:[1,1,0]
	v_pk_fma_f16 v107, v107, v104, s21 op_sel_hi:[1,1,0]
	v_pk_fma_f16 v106, v106, v105, s21 op_sel_hi:[1,1,0]
	v_pk_fma_f16 v108, v108, v103, s21 op_sel_hi:[1,1,0]
	v_pk_fma_f16 v109, v109, v102, s21 op_sel_hi:[1,1,0]
	v_pk_max_f16 v98, v98, 0
	v_pk_max_f16 v99, v99, 0
	v_pk_max_f16 v100, v100, 0
	v_pk_max_f16 v101, v101, 0
	v_exp_f16_e32 v119, v106
	v_exp_f16_e32 v120, v107
	v_exp_f16_e32 v121, v108
	v_exp_f16_e32 v122, v109
	v_exp_f16_sdwa v119, v106 dst_sel:WORD_1 dst_unused:UNUSED_PRESERVE src0_sel:WORD_1
	v_exp_f16_sdwa v120, v107 dst_sel:WORD_1 dst_unused:UNUSED_PRESERVE src0_sel:WORD_1
	v_exp_f16_sdwa v121, v108 dst_sel:WORD_1 dst_unused:UNUSED_PRESERVE src0_sel:WORD_1
	v_exp_f16_sdwa v122, v109 dst_sel:WORD_1 dst_unused:UNUSED_PRESERVE src0_sel:WORD_1
	s_nop 0
	v_pk_fma_f16 v101, v102, v122, v101
	v_pk_fma_f16 v100, v103, v121, v100
	v_pk_fma_f16 v99, v104, v120, v99
	v_pk_fma_f16 v98, v105, v119, v98
	ds_read_b128 v[102:105], v118 offset:192
	ds_read_b128 v[106:109], v218 offset:6144
	v_mfma_f32_32x32x16_f16 v[82:97], v[110:113], v[98:101], v[82:97]
	s_waitcnt lgkmcnt(1)
	v_pk_add_f16 v102, v174, v102
	v_pk_add_f16 v103, v175, v103
	v_pk_add_f16 v104, v176, v104
	v_pk_add_f16 v105, v177, v105
	v_or_b32_e32 v111, 0x80008000, v104
	v_mfma_f32_32x32x16_f16 v[66:81], v[114:117], v[98:101], v[66:81]
	v_or_b32_e32 v110, 0x80008000, v105
	v_or_b32_e32 v112, 0x80008000, v103
	v_or_b32_e32 v113, 0x80008000, v102
	v_pk_fma_f16 v114, v113, s3, v221 op_sel_hi:[1,0,0]
	v_pk_fma_f16 v115, v112, s3, v221 op_sel_hi:[1,0,0]
	v_pk_fma_f16 v116, v111, s3, v221 op_sel_hi:[1,0,0]
	v_pk_fma_f16 v117, v110, s3, v221 op_sel_hi:[1,0,0]
	ds_read_b128 v[98:101], v118 offset:224
	v_pk_fma_f16 v117, v117, v110, s20 op_sel_hi:[1,1,0]
	v_pk_fma_f16 v116, v116, v111, s20 op_sel_hi:[1,1,0]
	v_pk_fma_f16 v115, v115, v112, s20 op_sel_hi:[1,1,0]
	v_pk_fma_f16 v114, v114, v113, s20 op_sel_hi:[1,1,0]
	v_pk_max_f16 v102, v102, 0
	v_pk_max_f16 v103, v103, 0
	v_pk_max_f16 v104, v104, 0
	v_pk_max_f16 v105, v105, 0
	v_pk_fma_f16 v114, v114, v113, s21 op_sel_hi:[1,1,0]
	v_pk_fma_f16 v115, v115, v112, s21 op_sel_hi:[1,1,0]
	v_pk_fma_f16 v116, v116, v111, s21 op_sel_hi:[1,1,0]
	v_pk_fma_f16 v117, v117, v110, s21 op_sel_hi:[1,1,0]
	s_waitcnt lgkmcnt(0)
	v_pk_add_f16 v98, v178, v98
	ds_read_b128 v[242:245], v218 offset:16384
	ds_read_b128 v[246:249], v218 offset:17408
	ds_read_b128 v[250:253], v218 offset:18432
	v_exp_f16_e32 v118, v114
	v_exp_f16_e32 v119, v115
	v_exp_f16_e32 v120, v116
	v_exp_f16_e32 v121, v117
	v_exp_f16_sdwa v118, v114 dst_sel:WORD_1 dst_unused:UNUSED_PRESERVE src0_sel:WORD_1
	v_exp_f16_sdwa v119, v115 dst_sel:WORD_1 dst_unused:UNUSED_PRESERVE src0_sel:WORD_1
	v_exp_f16_sdwa v120, v116 dst_sel:WORD_1 dst_unused:UNUSED_PRESERVE src0_sel:WORD_1
	v_exp_f16_sdwa v121, v117 dst_sel:WORD_1 dst_unused:UNUSED_PRESERVE src0_sel:WORD_1
	v_pk_add_f16 v99, v179, v99
	v_pk_fma_f16 v105, v110, v121, v105
	v_pk_fma_f16 v104, v111, v120, v104
	v_pk_fma_f16 v103, v112, v119, v103
	v_pk_fma_f16 v102, v113, v118, v102
	ds_read_b128 v[110:113], v218 offset:7168
	v_pk_add_f16 v100, v180, v100
	v_mfma_f32_32x32x16_f16 v[82:97], v[106:109], v[102:105], v[82:97]
	ds_read_b128 v[106:109], v218 offset:14336
	ds_read_b128 v[114:117], v218 offset:15360
	v_pk_add_f16 v101, v181, v101
	s_waitcnt lgkmcnt(1)
	v_mfma_f32_32x32x16_f16 v[66:81], v[106:109], v[102:105], v[66:81]
	v_or_b32_e32 v102, 0x80008000, v101
	v_or_b32_e32 v103, 0x80008000, v100
	v_or_b32_e32 v104, 0x80008000, v99
	v_or_b32_e32 v105, 0x80008000, v98
	v_pk_fma_f16 v106, v105, s3, v221 op_sel_hi:[1,0,0]
	v_pk_fma_f16 v107, v104, s3, v221 op_sel_hi:[1,0,0]
	v_pk_fma_f16 v108, v103, s3, v221 op_sel_hi:[1,0,0]
	v_pk_fma_f16 v109, v102, s3, v221 op_sel_hi:[1,0,0]
	v_pk_fma_f16 v108, v108, v103, s20 op_sel_hi:[1,1,0]
	v_pk_fma_f16 v109, v109, v102, s20 op_sel_hi:[1,1,0]
	v_pk_fma_f16 v107, v107, v104, s20 op_sel_hi:[1,1,0]
	v_pk_fma_f16 v106, v106, v105, s20 op_sel_hi:[1,1,0]
	v_pk_max_f16 v98, v98, 0
	v_pk_max_f16 v99, v99, 0
	v_pk_max_f16 v100, v100, 0
	v_pk_max_f16 v101, v101, 0
	v_pk_fma_f16 v106, v106, v105, s21 op_sel_hi:[1,1,0]
	v_pk_fma_f16 v107, v107, v104, s21 op_sel_hi:[1,1,0]
	v_pk_fma_f16 v108, v108, v103, s21 op_sel_hi:[1,1,0]
	v_pk_fma_f16 v109, v109, v102, s21 op_sel_hi:[1,1,0]
	s_nop 0
	v_exp_f16_e32 v118, v106
	v_exp_f16_e32 v119, v107
	v_exp_f16_e32 v120, v108
	v_exp_f16_e32 v121, v109
	v_exp_f16_sdwa v118, v106 dst_sel:WORD_1 dst_unused:UNUSED_PRESERVE src0_sel:WORD_1
	v_exp_f16_sdwa v119, v107 dst_sel:WORD_1 dst_unused:UNUSED_PRESERVE src0_sel:WORD_1
	v_exp_f16_sdwa v120, v108 dst_sel:WORD_1 dst_unused:UNUSED_PRESERVE src0_sel:WORD_1
	v_exp_f16_sdwa v121, v109 dst_sel:WORD_1 dst_unused:UNUSED_PRESERVE src0_sel:WORD_1
	s_nop 0
	v_pk_fma_f16 v101, v102, v121, v101
	v_pk_fma_f16 v100, v103, v120, v100
	v_pk_fma_f16 v99, v104, v119, v99
	v_pk_fma_f16 v98, v105, v118, v98
	s_nop 1
	v_mfma_f32_32x32x16_f16 v[82:97], v[110:113], v[98:101], v[82:97]
	s_waitcnt lgkmcnt(0)
	v_mfma_f32_32x32x16_f16 v[66:81], v[114:117], v[98:101], v[66:81]
	s_setprio 1
	ds_read_b128 v[98:101], v222 offset:4096
	ds_read_b128 v[102:105], v222 offset:5120
	ds_read_b128 v[106:109], v222 offset:6144
	ds_read_b128 v[110:113], v222 offset:7168
	s_nop 4
	v_cvt_pk_f16_f32 v114, v82, v83
	v_cvt_pk_f16_f32 v115, v84, v85
	v_cvt_pk_f16_f32 v116, v86, v87
	v_cvt_pk_f16_f32 v117, v88, v89
	v_pk_add_f16 v126, v126, v114
	v_pk_add_f16 v127, v127, v115
	v_pk_add_f16 v128, v128, v116
	v_pk_add_f16 v129, v129, v117
	s_nop 1
	v_mfma_f32_32x32x16_f16 v[226:241], v[242:245], v[126:129], v[226:241]
	ds_read_b128 v[242:245], v218 offset:21504
	v_cvt_pk_f16_f32 v118, v90, v91
	v_cvt_pk_f16_f32 v119, v92, v93
	v_cvt_pk_f16_f32 v120, v94, v95
	v_cvt_pk_f16_f32 v121, v96, v97
	v_pk_add_f16 v130, v130, v118
	v_pk_add_f16 v131, v131, v119
	v_pk_add_f16 v132, v132, v120
	v_pk_add_f16 v133, v133, v121
	s_nop 1
	v_mfma_f32_32x32x16_f16 v[226:241], v[246:249], v[130:133], v[226:241]
	ds_read_b128 v[246:249], v218 offset:22528
	v_cvt_pk_f16_f32 v122, v66, v67
	v_cvt_pk_f16_f32 v123, v68, v69
	v_cvt_pk_f16_f32 v124, v70, v71
	v_cvt_pk_f16_f32 v125, v72, v73
	v_pk_add_f16 v134, v134, v122
	v_pk_add_f16 v135, v135, v123
	v_pk_add_f16 v136, v136, v124
	v_pk_add_f16 v137, v137, v125
	s_nop 1
	v_mfma_f32_32x32x16_f16 v[226:241], v[250:253], v[134:137], v[226:241]
	ds_read_b128 v[250:253], v218 offset:23552
	v_cvt_pk_f16_f32 v182, v74, v75
	v_cvt_pk_f16_f32 v183, v76, v77
	v_cvt_pk_f16_f32 v184, v78, v79
	v_cvt_pk_f16_f32 v185, v80, v81
	v_pk_add_f16 v138, v138, v182
	v_pk_add_f16 v139, v139, v183
	v_pk_add_f16 v140, v140, v184
	v_pk_add_f16 v141, v141, v185
	s_nop 1
	v_mfma_f32_32x32x16_f16 v[226:241], v[150:153], v[138:141], v[226:241]
	ds_read_b128 v[150:153], v218 offset:24576
	ds_read_b128 v[66:69], v222 offset:8192
	ds_read_b128 v[70:73], v222 offset:9216
	ds_read_b128 v[74:77], v222 offset:10240
	ds_read_b128 v[78:81], v222 offset:11264
	ds_read_b128 v[82:85], v222 offset:12288
	ds_read_b128 v[86:89], v222 offset:13312
	ds_read_b128 v[90:93], v222 offset:14336
	ds_read_b128 v[94:97], v222 offset:15360
	s_waitcnt lgkmcnt(12)
	v_mfma_f32_32x32x16_f16 v[98:113], v[154:157], v[126:129], v[98:113]
	ds_read_b128 v[154:157], v218 offset:25600
	s_waitcnt lgkmcnt(12)
	v_mfma_f32_32x32x16_f16 v[98:113], v[242:245], v[130:133], v[98:113]
	ds_read_b128 v[242:245], v218 offset:26624
	s_waitcnt lgkmcnt(12)
	v_mfma_f32_32x32x16_f16 v[98:113], v[246:249], v[134:137], v[98:113]
	ds_read_b128 v[246:249], v218 offset:27648
	v_cvt_pk_f16_f32 v226, v226, v227
	v_cvt_pk_f16_f32 v227, v228, v229
	v_cvt_pk_f16_f32 v228, v230, v231
	v_cvt_pk_f16_f32 v229, v232, v233
	v_pk_max_f16 v226, v226, 0
	v_pk_max_f16 v227, v227, 0
	v_pk_max_f16 v228, v228, 0
	v_pk_max_f16 v229, v229, 0
	s_waitcnt lgkmcnt(12)
	v_mfma_f32_32x32x16_f16 v[98:113], v[250:253], v[138:141], v[98:113]
	ds_read_b128 v[250:253], v218 offset:28672
	v_cvt_pk_f16_f32 v230, v234, v235
	v_cvt_pk_f16_f32 v231, v236, v237
	v_cvt_pk_f16_f32 v232, v238, v239
	v_cvt_pk_f16_f32 v233, v240, v241
	v_pk_max_f16 v230, v230, 0
	v_pk_max_f16 v231, v231, 0
	v_pk_max_f16 v232, v232, 0
	v_pk_max_f16 v233, v233, 0
	s_waitcnt lgkmcnt(8)
	v_mfma_f32_32x32x16_f16 v[66:81], v[150:153], v[126:129], v[66:81]
	ds_read_b128 v[150:153], v218 offset:29696
	s_waitcnt lgkmcnt(4)
	v_mfma_f32_32x32x16_f16 v[66:81], v[154:157], v[130:133], v[66:81]
	ds_read_b128 v[154:157], v218 offset:30720
	s_waitcnt lgkmcnt(4)
	v_mfma_f32_32x32x16_f16 v[66:81], v[242:245], v[134:137], v[66:81]
	ds_read_b128 v[242:245], v218 offset:31744
	v_cvt_pk_f16_f32 v98, v98, v99
	v_cvt_pk_f16_f32 v99, v100, v101
	v_cvt_pk_f16_f32 v100, v102, v103
	v_cvt_pk_f16_f32 v101, v104, v105
	v_pk_max_f16 v98, v98, 0
	v_pk_max_f16 v99, v99, 0
	v_pk_max_f16 v100, v100, 0
	v_pk_max_f16 v101, v101, 0
	s_waitcnt lgkmcnt(4)
	v_mfma_f32_32x32x16_f16 v[66:81], v[246:249], v[138:141], v[66:81]
	ds_read_b128 v[246:249], v218 offset:32768
	v_cvt_pk_f16_f32 v102, v106, v107
	v_cvt_pk_f16_f32 v103, v108, v109
	v_cvt_pk_f16_f32 v104, v110, v111
	v_cvt_pk_f16_f32 v105, v112, v113
	v_pk_max_f16 v102, v102, 0
	v_pk_max_f16 v103, v103, 0
	v_pk_max_f16 v104, v104, 0
	v_pk_max_f16 v105, v105, 0
	s_waitcnt lgkmcnt(4)
	v_mfma_f32_32x32x16_f16 v[82:97], v[250:253], v[126:129], v[82:97]
	ds_read_b128 v[250:253], v218 offset:33792
	s_waitcnt lgkmcnt(4)
	v_mfma_f32_32x32x16_f16 v[82:97], v[150:153], v[130:133], v[82:97]
	ds_read_b128 v[150:153], v218 offset:34816
	s_waitcnt lgkmcnt(4)
	v_mfma_f32_32x32x16_f16 v[82:97], v[154:157], v[134:137], v[82:97]
	ds_read_b128 v[154:157], v218 offset:35840
	v_cvt_pk_f16_f32 v66, v66, v67
	v_cvt_pk_f16_f32 v67, v68, v69
	v_cvt_pk_f16_f32 v68, v70, v71
	v_cvt_pk_f16_f32 v69, v72, v73
	v_pk_max_f16 v66, v66, 0
	v_pk_max_f16 v67, v67, 0
	v_pk_max_f16 v68, v68, 0
	v_pk_max_f16 v69, v69, 0
	s_waitcnt lgkmcnt(4)
	v_mfma_f32_32x32x16_f16 v[82:97], v[242:245], v[138:141], v[82:97]
	ds_read_b128 v[242:245], v218 offset:36864
	v_cvt_pk_f16_f32 v70, v74, v75
	v_cvt_pk_f16_f32 v71, v76, v77
	v_cvt_pk_f16_f32 v72, v78, v79
	v_cvt_pk_f16_f32 v73, v80, v81
	v_pk_max_f16 v70, v70, 0
	v_pk_max_f16 v71, v71, 0
	v_pk_max_f16 v72, v72, 0
	v_pk_max_f16 v73, v73, 0
	s_waitcnt lgkmcnt(4)
	v_mfma_f32_32x32x16_f16 v[126:141], v[246:249], v[226:229], v[2:17]
	ds_read_b128 v[246:249], v218 offset:37888
	s_waitcnt lgkmcnt(4)
	v_mfma_f32_32x32x16_f16 v[126:141], v[250:253], v[230:233], v[126:141]
	ds_read_b128 v[250:253], v218 offset:38912
	s_waitcnt lgkmcnt(4)
	v_mfma_f32_32x32x16_f16 v[126:141], v[150:153], v[98:101], v[126:141]
	ds_read_b128 v[150:153], v218 offset:39936
	s_waitcnt lgkmcnt(4)
	v_mfma_f32_32x32x16_f16 v[126:141], v[154:157], v[102:105], v[126:141]
	ds_read_b128 v[154:157], v218 offset:40960
	s_waitcnt lgkmcnt(4)
	v_mfma_f32_32x32x16_f16 v[126:141], v[242:245], v[66:69], v[126:141]
	ds_read_b128 v[242:245], v218 offset:41984
	v_cvt_pk_f16_f32 v97, v96, v97
	v_cvt_pk_f16_f32 v96, v94, v95
	v_cvt_pk_f16_f32 v95, v92, v93
	v_cvt_pk_f16_f32 v94, v90, v91
	v_pk_max_f16 v97, v97, 0
	v_pk_max_f16 v96, v96, 0
	v_pk_max_f16 v95, v95, 0
	v_pk_max_f16 v94, v94, 0
	s_waitcnt lgkmcnt(4)
	v_mfma_f32_32x32x16_f16 v[126:141], v[246:249], v[70:73], v[126:141]
	ds_read_b128 v[246:249], v218 offset:43008
	v_cvt_pk_f16_f32 v93, v88, v89
	v_cvt_pk_f16_f32 v92, v86, v87
	v_cvt_pk_f16_f32 v91, v84, v85
	v_cvt_pk_f16_f32 v90, v82, v83
	v_pk_max_f16 v93, v93, 0
	v_pk_max_f16 v92, v92, 0
	v_pk_max_f16 v91, v91, 0
	v_pk_max_f16 v90, v90, 0
	s_waitcnt lgkmcnt(4)
	s_nop 0
	v_mfma_f32_32x32x16_f16 v[126:141], v[250:253], v[90:93], v[126:141]
	ds_read_b128 v[250:253], v218 offset:44032
	s_waitcnt lgkmcnt(4)
	v_mfma_f32_32x32x16_f16 v[126:141], v[150:153], v[94:97], v[126:141]
	ds_read_b128 v[150:153], v218 offset:45056
	s_waitcnt lgkmcnt(4)
	v_mfma_f32_32x32x16_f16 v[74:89], v[154:157], v[226:229], v[34:49]
	ds_read_b128 v[154:157], v218 offset:46080
	s_waitcnt lgkmcnt(4)
	v_mfma_f32_32x32x16_f16 v[74:89], v[242:245], v[230:233], v[74:89]
	ds_read_b128 v[242:245], v218 offset:47104
	s_waitcnt lgkmcnt(4)
	v_mfma_f32_32x32x16_f16 v[74:89], v[246:249], v[98:101], v[74:89]
	ds_read_b128 v[246:249], v218 offset:48128
	s_waitcnt lgkmcnt(4)
	v_mfma_f32_32x32x16_f16 v[74:89], v[250:253], v[102:105], v[74:89]
	s_waitcnt lgkmcnt(3)
	v_mfma_f32_32x32x16_f16 v[74:89], v[150:153], v[66:69], v[74:89]
	ds_read_b128 v[150:153], v218
	v_max3_f32 v254, v126, v127, v128
	v_max3_f32 v255, v129, v130, v131
	v_max3_f32 v254, v254, v132, v133
	v_max3_f32 v255, v255, v134, v135
	v_max3_f32 v254, v254, v136, v137
	v_max3_f32 v255, v255, v138, v139
	v_max3_f32 v254, v254, v140, v141
	v_max_f32_e32 v254, v254, v255
	v_cmp_lt_f32_e32 vcc, s5, v254
	s_cbranch_vccz .Lm_norescale0
	v_max_f32_e32 v234, 0, v126
	v_max_f32_e32 v235, 0, v127
	v_max_f32_e32 v236, 0, v128
	v_max_f32_e32 v237, 0, v129
	v_max_f32_e32 v238, 0, v130
	v_max_f32_e32 v239, 0, v131
	v_max_f32_e32 v240, 0, v132
	v_max_f32_e32 v241, 0, v133
	v_max_f32_e32 v106, 0, v134
	v_max_f32_e32 v107, 0, v135
	v_max_f32_e32 v108, 0, v136
	v_max_f32_e32 v109, 0, v137
	v_max_f32_e32 v110, 0, v138
	v_max_f32_e32 v111, 0, v139
	v_max_f32_e32 v112, 0, v140
	v_max_f32_e32 v113, 0, v141
	v_sub_f32_e32 v126, v126, v234
	v_sub_f32_e32 v127, v127, v235
	v_sub_f32_e32 v128, v128, v236
	v_sub_f32_e32 v129, v129, v237
	v_sub_f32_e32 v130, v130, v238
	v_sub_f32_e32 v131, v131, v239
	v_sub_f32_e32 v132, v132, v240
	v_sub_f32_e32 v133, v133, v241
	v_sub_f32_e32 v134, v134, v106
	v_sub_f32_e32 v135, v135, v107
	v_sub_f32_e32 v136, v136, v108
	v_sub_f32_e32 v137, v137, v109
	v_sub_f32_e32 v138, v138, v110
	v_sub_f32_e32 v139, v139, v111
	v_sub_f32_e32 v140, v140, v112
	v_sub_f32_e32 v141, v141, v113
	v_sub_f32_e32 v2, v2, v234
	v_sub_f32_e32 v3, v3, v235
	v_sub_f32_e32 v4, v4, v236
	v_sub_f32_e32 v5, v5, v237
	v_sub_f32_e32 v6, v6, v238
	v_sub_f32_e32 v7, v7, v239
	v_sub_f32_e32 v8, v8, v240
	v_sub_f32_e32 v9, v9, v241
	v_sub_f32_e32 v10, v10, v106
	v_sub_f32_e32 v11, v11, v107
	v_sub_f32_e32 v12, v12, v108
	v_sub_f32_e32 v13, v13, v109
	v_sub_f32_e32 v14, v14, v110
	v_sub_f32_e32 v15, v15, v111
	v_sub_f32_e32 v16, v16, v112
	v_sub_f32_e32 v17, v17, v113
	v_exp_f32_e64 v234, -v234
	v_exp_f32_e64 v235, -v235
	v_exp_f32_e64 v236, -v236
	v_exp_f32_e64 v237, -v237
	v_exp_f32_e64 v238, -v238
	v_exp_f32_e64 v239, -v239
	v_exp_f32_e64 v240, -v240
	v_exp_f32_e64 v241, -v241
	v_exp_f32_e64 v106, -v106
	v_exp_f32_e64 v107, -v107
	v_exp_f32_e64 v108, -v108
	v_exp_f32_e64 v109, -v109
	v_exp_f32_e64 v110, -v110
	v_exp_f32_e64 v111, -v111
	v_exp_f32_e64 v112, -v112
	v_exp_f32_e64 v113, -v113
	s_nop 0
	v_mul_f32_e32 v50, v234, v50
	v_mul_f32_e32 v51, v235, v51
	v_mul_f32_e32 v52, v236, v52
	v_mul_f32_e32 v53, v237, v53
	v_mul_f32_e32 v54, v238, v54
	v_mul_f32_e32 v55, v239, v55
	v_mul_f32_e32 v56, v240, v56
	v_mul_f32_e32 v57, v241, v57
	v_mul_f32_e32 v58, v106, v58
	v_mul_f32_e32 v59, v107, v59
	v_mul_f32_e32 v60, v108, v60
	v_mul_f32_e32 v61, v109, v61
	v_mul_f32_e32 v62, v110, v62
	v_mul_f32_e32 v63, v111, v63
	v_mul_f32_e32 v64, v112, v64
	v_mul_f32_e32 v65, v113, v65
	v_mul_f32_e32 v216, v234, v216
	v_mul_f32_e32 v217, v235, v217
	v_mul_f32_e32 v214, v236, v214
	v_mul_f32_e32 v215, v237, v215
	v_mul_f32_e32 v212, v238, v212
	v_mul_f32_e32 v213, v239, v213
	v_mul_f32_e32 v210, v240, v210
	v_mul_f32_e32 v211, v241, v211
	v_mul_f32_e32 v208, v106, v208
	v_mul_f32_e32 v209, v107, v209
	v_mul_f32_e32 v204, v108, v204
	v_mul_f32_e32 v205, v109, v205
	v_mul_f32_e32 v202, v110, v202
	v_mul_f32_e32 v203, v111, v203
	v_mul_f32_e32 v196, v112, v196
	v_mul_f32_e32 v197, v113, v197
	s_nop 1

.Lm_norescale1:
	v_exp_f32_e32 v234, v74
	v_exp_f32_e32 v235, v75
	v_exp_f32_e32 v236, v76
	v_exp_f32_e32 v237, v77
	v_exp_f32_e32 v238, v78
	v_exp_f32_e32 v239, v79
	v_exp_f32_e32 v240, v80
	v_exp_f32_e32 v241, v81
	v_exp_f32_e32 v106, v82
	v_exp_f32_e32 v107, v83
	v_exp_f32_e32 v108, v84
	v_exp_f32_e32 v109, v85
	v_exp_f32_e32 v110, v86
	v_exp_f32_e32 v111, v87
	v_exp_f32_e32 v112, v88
	v_exp_f32_e32 v113, v89
	v_pk_add_f32 v[18:19], v[234:235], v[18:19]
	v_pk_add_f32 v[20:21], v[236:237], v[20:21]
	v_pk_add_f32 v[22:23], v[238:239], v[22:23]
	v_pk_add_f32 v[24:25], v[240:241], v[24:25]
	v_pk_add_f32 v[26:27], v[106:107], v[26:27]
	v_pk_add_f32 v[28:29], v[108:109], v[28:29]
	v_pk_add_f32 v[30:31], v[110:111], v[30:31]
	v_pk_add_f32 v[32:33], v[112:113], v[32:33]
	v_fma_mix_f32 v206, v234, v122, v206 op_sel:[0,0,0] op_sel_hi:[0,1,0]
	v_fma_mix_f32 v207, v235, v122, v207 op_sel:[0,1,0] op_sel_hi:[0,1,0]
	v_fma_mix_f32 v200, v236, v123, v200 op_sel:[0,0,0] op_sel_hi:[0,1,0]
	v_fma_mix_f32 v201, v237, v123, v201 op_sel:[0,1,0] op_sel_hi:[0,1,0]
	v_fma_mix_f32 v198, v238, v124, v198 op_sel:[0,0,0] op_sel_hi:[0,1,0]
	v_fma_mix_f32 v199, v239, v124, v199 op_sel:[0,1,0] op_sel_hi:[0,1,0]
	v_fma_mix_f32 v194, v240, v125, v194 op_sel:[0,0,0] op_sel_hi:[0,1,0]
	v_fma_mix_f32 v195, v241, v125, v195 op_sel:[0,1,0] op_sel_hi:[0,1,0]
	v_fma_mix_f32 v192, v106, v182, v192 op_sel:[0,0,0] op_sel_hi:[0,1,0]
	v_fma_mix_f32 v193, v107, v182, v193 op_sel:[0,1,0] op_sel_hi:[0,1,0]
	v_fma_mix_f32 v190, v108, v183, v190 op_sel:[0,0,0] op_sel_hi:[0,1,0]
	v_fma_mix_f32 v191, v109, v183, v191 op_sel:[0,1,0] op_sel_hi:[0,1,0]
	v_fma_mix_f32 v188, v110, v184, v188 op_sel:[0,0,0] op_sel_hi:[0,1,0]
	v_fma_mix_f32 v189, v111, v184, v189 op_sel:[0,1,0] op_sel_hi:[0,1,0]
	v_fma_mix_f32 v186, v112, v185, v186 op_sel:[0,0,0] op_sel_hi:[0,1,0]
	v_fma_mix_f32 v187, v113, v185, v187 op_sel:[0,1,0] op_sel_hi:[0,1,0]
	s_addk_i32 s4, 0x280
	s_cmpk_eq_i32 s4, 0x2080
	s_cbranch_scc0 .LBB1_14
	s_waitcnt lgkmcnt(0)
